# gather static priority raise at level 3 (instead of 1) for the favoured wave half
# baseline (speedup 1.0000x reference)
; __device__ __forceinline__ int fresh_lane() { unsigned z = 0u; asm volatile("" : "+v"(z)); return (int)__builtin_amdgcn_mbcnt_hi(~0u, __builtin_amdgcn_mbcnt_lo(~0u, z)); }
;     const unsigned char* UV4 = (const unsigned char*)(F.ws + WS_UB) + (size_t)layer * (2u * TAB4);
;     const bf16* ZB = (const bf16*)(F.ws + WS_ZF); const bf16* PLE = (const bf16*)(F.ws + WS_PLE);
;     const int* IDX = (const int*)(F.ws + WS_IDX); const float* GWt = (const float*)(F.ws + WS_GW);
;     float* OF = (layer == 3 && !dummy) ? F.out : (float*)nullptr; bf16* XB = (bf16*)(F.ws + (dummy ? WS_X1B : WS_XB));
;     ...
;     const int idmask = (dummy == 1) ? PROBE_GATHER_MASK : 0x3fff;
;     ...
;     const float* gain1 = F.ln_gain + (size_t)(layer * 2) * D; const float* bias1 = F.ln_bias + (size_t)(layer * 2) * D;
;     const float* gain = F.ln_gain + (size_t)(layer * 2 + 1) * D; const float* bias = F.ln_bias + (size_t)(layer * 2 + 1) * D;
;     const int lane = fresh_lane();
;     const bool b3 = (lane & 8) != 0, b2 = (lane & 4) != 0, b1 = (lane & 2) != 0, b0 = (lane & 1) != 0;
;     const __amdgpu_buffer_rsrc_t rs = __builtin_amdgcn_make_buffer_rsrc((void*)UV4, (short)0, (int)(2u * TAB4), 0x00020000);
;     const unsigned voff = (unsigned)lane * 16u;
;     v4u ring[16];
;     int id0 = 0, id1 = 0, id0n = 0;
;     ...
;     int id1n = 0; float g0n = 0.f, g1n = 0.f;
;     if (F.gw < T) { gather_sorted_ids(IDX, GWt, F.gw, lane, id0n, id1n, g0n, g1n);
;     ...
;         id0n &= idmask; id1n &= idmask;
;     ...
; #pragma unroll
;         for (int k = 0; k < 16; ++k) GATHER_ISSUE(k, 256 + k); }
;     for (int t = F.gw; t < T; t += F.ngw) {
;         int xh[4], xl[4]; float xdq, mean1, rstd1;
;         {
;             const v4u hq = *(const v4u*)(F.ws + WS_XQ + (size_t)t * 2048 + lane * 32), lq = *(const v4u*)(F.ws + WS_XQ + (size_t)t * 2048 + lane * 32 + 16);
;             const f32x4 r4 = *(const f32x4*)(F.ws + WS_R4 + (size_t)t * 16);
;             xh[0] = (int)hq.x; xh[1] = (int)hq.y; xh[2] = (int)hq.z; xh[3] = (int)hq.w; xl[0] = (int)lq.x; xl[1] = (int)lq.y; xl[2] = (int)lq.z; xl[3] = (int)lq.w;
;             xdq = r4[0]; mean1 = r4[1]; rstd1 = r4[2];
;         }
;         if (t - F.wave + (NWAVES - 1) < T) __syncthreads();
;         id0 = id0n; id1 = id1n; const float g0 = g0n, g1 = g1n;
;         { const int tn = (t + F.ngw < T) ? t + F.ngw : t; gather_sorted_ids(IDX, GWt, tn, lane, id0n, id1n, g0n, g1n);
.LBB0_1412:
	s_andn2_b64 vcc, exec, s[14:15]
	s_cbranch_vccnz .LBB0_1452
	s_add_u32 s8, s60, 0x4a600000
	v_writelane_b32 v254, s8, 56
	s_addc_u32 s8, s61, 0
	v_writelane_b32 v255, s8, 5
	s_add_u32 s8, s60, 0x66600000
	v_writelane_b32 v255, s8, 7
	s_addc_u32 s8, s61, 0
	s_cmp_eq_u32 s18, 3
	v_writelane_b32 v255, s8, 9
	s_cselect_b64 s[8:9], -1, 0
	s_add_u32 s10, s60, 0x36600000
	v_writelane_b32 v255, s10, 11
	s_addc_u32 s43, s61, 0
	s_lshl_b32 s10, s18, 1
	s_mov_b64 s[16:17], s[80:81]
	v_writelane_b32 v255, s76, 1
	s_mov_b64 s[18:19], s[82:83]
	s_mov_b64 s[20:21], s[84:85]
	s_mov_b64 s[22:23], s[86:87]
	v_writelane_b32 v255, s77, 2
	v_readlane_b32 s76, v254, 1
	s_ashr_i32 s11, s10, 31
	v_readlane_b32 s90, v254, 15
	v_readlane_b32 s91, v254, 16
	s_lshl_b64 s[12:13], s[10:11], 13
	s_mov_b64 s[14:15], s[90:91]
	s_add_u32 s36, s14, s12
	s_addc_u32 s37, s15, s13
	s_add_u32 s12, s16, s12
	s_addc_u32 s13, s17, s13
	s_or_b32 s10, s10, 1
	v_readlane_b32 s72, v255, 1
	s_ashr_i32 s11, s10, 31
	v_readlane_b32 s73, v255, 2
	v_writelane_b32 v255, s12, 13
	s_lshl_b64 s[10:11], s[10:11], 13
	v_readlane_b32 s80, v254, 5
	v_writelane_b32 v255, s13, 14
	s_add_u32 s12, s14, s10
	s_addc_u32 s13, s15, s11
	v_readlane_b32 s81, v254, 6
	s_add_u32 s80, s16, s10
	s_addc_u32 s81, s17, s11
	v_readlane_b32 s10, v254, 51
	v_readlane_b32 s82, v254, 7
	v_readlane_b32 s83, v254, 8
	v_readlane_b32 s11, v254, 52
	s_and_b64 s[82:83], s[8:9], s[10:11]
	s_add_u32 s30, s60, 0x57600000
	v_writelane_b32 v255, s12, 15
	s_addc_u32 s39, s61, 0
	s_add_u32 s8, s60, 0x53200000
	v_writelane_b32 v255, s13, 16
	v_writelane_b32 v255, s8, 33
	s_addc_u32 s8, s61, 0
	v_writelane_b32 v255, s8, 35
	s_add_u32 s8, s60, 0x53600000
	v_writelane_b32 v255, s8, 29
	s_addc_u32 s8, s61, 0
	v_cmp_eq_u32_e64 s[28:29], 0, v68
	v_cmp_eq_u32_e32 vcc, 0, v67
	v_writelane_b32 v255, s8, 31
	s_xor_b64 s[44:45], vcc, s[28:29]
	v_cmp_eq_u32_e64 s[20:21], 0, v69
	v_writelane_b32 v255, s44, 17
	v_lshlrev_b32_e32 v70, 5, v130
	v_ashrrev_i32_e32 v71, 31, v70
	v_writelane_b32 v255, s45, 18
	s_xor_b64 s[44:45], vcc, s[20:21]
	v_writelane_b32 v255, s44, 19
	v_add_u32_e32 v194, 4, v66
	v_add_u32_e32 v195, 8, v66
	v_writelane_b32 v255, s45, 20
	s_xor_b64 s[44:45], vcc, s[0:1]
	v_writelane_b32 v255, s44, 21
	v_add_u32_e32 v196, 12, v66
	v_lshl_add_u64 v[66:67], s[60:61], 0, v[70:71]
	v_writelane_b32 v255, s45, 22
	s_xor_b64 s[44:45], vcc, s[2:3]
	v_writelane_b32 v255, s44, 23
	s_xor_b64 s[8:9], s[4:5], s[6:7]
	s_xor_b64 s[10:11], s[2:3], s[4:5]
	v_writelane_b32 v255, s45, 24
	s_xor_b64 s[44:45], vcc, s[4:5]
	v_writelane_b32 v255, s44, 25
	s_xor_b64 s[12:13], s[2:3], s[6:7]
	s_xor_b64 s[14:15], s[0:1], s[2:3]
	v_writelane_b32 v255, s45, 26
	s_xor_b64 s[44:45], vcc, s[6:7]
	v_writelane_b32 v255, s44, 27
	s_xor_b64 s[16:17], s[0:1], s[4:5]
	s_xor_b64 s[18:19], s[0:1], s[6:7]
	v_writelane_b32 v255, s45, 28
	s_mov_b64 s[44:45], 0x55600000
	s_xor_b64 s[22:23], s[20:21], s[0:1]
	s_xor_b64 s[24:25], s[20:21], s[2:3]
	s_xor_b64 s[26:27], s[20:21], s[4:5]
	v_ashrrev_i32_e32 v193, 4, v130
	v_lshl_add_u64 v[132:133], v[66:67], 0, s[44:45]
	s_xor_b64 s[44:45], s[20:21], s[6:7]
	s_xor_b64 s[46:47], s[28:29], s[20:21]
	s_xor_b64 s[48:49], s[28:29], s[0:1]
	s_xor_b64 s[50:51], s[28:29], s[2:3]
	s_xor_b64 s[52:53], s[28:29], s[4:5]
	s_xor_b64 s[54:55], s[28:29], s[6:7]
	v_readlane_b32 s77, v254, 2
	v_readlane_b32 s78, v254, 3
	v_readlane_b32 s79, v254, 4
	v_readlane_b32 s84, v254, 9
	v_readlane_b32 s85, v254, 10
	v_readlane_b32 s86, v254, 11
	v_readlane_b32 s87, v254, 12
	v_readlane_b32 s88, v254, 13
	v_readlane_b32 s89, v254, 14
	v_readlane_b32 s98, v254, 55
	s_lshl_b32 s98, s98, 6
	v_add_u32_e32 v228, s98, v130
	v_lshlrev_b32_e32 v228, 4, v228
	global_load_dwordx4 v[212:215], v228, s[36:37]
	global_load_dwordx4 v[224:227], v228, s[80:81]
	v_readlane_b32 s98, v255, 13
	v_readlane_b32 s99, v255, 14
	s_nop 4
	global_load_dwordx4 v[216:219], v228, s[98:99]
	v_readlane_b32 s98, v255, 15
	v_readlane_b32 s99, v255, 16
	s_nop 4
	global_load_dwordx4 v[220:223], v228, s[98:99]
	s_waitcnt vmcnt(3)
	ds_write_b128 v228, v[212:215]
	s_waitcnt vmcnt(2)
	ds_write_b128 v228, v[224:227] offset:24576
	s_waitcnt vmcnt(1)
	ds_write_b128 v228, v[216:219] offset:8192
	s_waitcnt vmcnt(0)
	ds_write_b128 v228, v[220:223] offset:16384
	s_waitcnt lgkmcnt(0)
	s_barrier
	v_readlane_b32 s100, v254, 58
	v_readlane_b32 s99, v255, 1
	s_add_i32 s99, s100, s99
	s_cmp_lt_i32 s99, 0x4000
	s_cselect_b32 s99, s99, s100
	s_lshl_b32 s100, s100, 12
	s_lshl_b32 s99, s99, 9
	v_lshl_add_u32 v244, v130, 6, s100
	v_lshl_add_u32 v249, v130, 2, s99
	v_readlane_b32 s100, v255, 7
	v_readlane_b32 s101, v255, 9
	s_nop 4
	global_load_dwordx4 v[212:215], v244, s[100:101] offset:48
	global_load_dwordx4 v[216:219], v244, s[100:101] offset:32
	global_load_dwordx4 v[220:223], v244, s[100:101] offset:16
	global_load_dwordx4 v[224:227], v244, s[100:101]
	v_readlane_b32 s100, v254, 56
	v_readlane_b32 s101, v255, 5
	s_nop 4
	global_load_dwordx4 v[228:231], v244, s[100:101] offset:48
	global_load_dwordx4 v[232:235], v244, s[100:101] offset:32
	global_load_dwordx4 v[236:239], v244, s[100:101] offset:16
	global_load_dwordx4 v[240:243], v244, s[100:101]
	global_load_dword v245, v249, s[70:71] offset:256
	global_load_dword v246, v249, s[40:41] offset:256
	global_load_dword v247, v249, s[40:41]
	global_load_dword v248, v249, s[70:71]
	v_readlane_b32 s98, v254, 55
	s_cmp_lt_u32 s98, 4
	s_cbranch_scc1 .Lprio_lo
	s_setprio 3
